# speedup vs baseline: 1.0271x; 1.0008x over previous
.LBB2_137:
	v_lshlrev_b32_e32 v20, 2, v22
	global_load_dwordx4 v[26:29], v20, s[20:21]
	v_add_u32_e32 v25, s18, v22
	v_lshl_add_u64 v[18:19], v[0:1], 2, s[4:5]
	v_mov_b32_e32 v21, 0
	v_or_b32_e32 v24, 16, v22
	v_mad_i64_i32 v[30:31], s[2:3], v25, s34, 0
	v_add_u32_e32 v32, 1, v25
	v_add_u32_e32 v34, 2, v25
	v_add_u32_e32 v25, 3, v25
	v_lshl_add_u64 v[20:21], s[20:21], 0, v[20:21]
	v_lshl_add_u64 v[30:31], v[30:31], 2, v[18:19]
	v_mad_i64_i32 v[32:33], s[2:3], v32, s34, 0
	v_mad_i64_i32 v[34:35], s[2:3], v34, s34, 0
	v_mad_i64_i32 v[36:37], s[2:3], v25, s34, 0
	v_cmp_gt_u32_e32 vcc, 20, v24
	v_lshl_add_u64 v[32:33], v[32:33], 2, v[18:19]
	v_lshl_add_u64 v[34:35], v[34:35], 2, v[18:19]
	v_lshl_add_u64 v[36:37], v[36:37], 2, v[18:19]
	s_and_saveexec_b64 s[68:69], vcc
	global_load_dword v114, v[20:21], off offset:64
	global_load_dword v115, v[20:21], off offset:68
	global_load_dword v116, v[20:21], off offset:72
	s_mov_b64 exec, s[68:69]
	s_waitcnt vmcnt(0)
	v_add_f32_e32 v14, v14, v26
	v_add_f32_e32 v15, v15, v27
	v_add_f32_e32 v16, v16, v28
	v_add_f32_e32 v17, v17, v29
	global_store_dword v[30:31], v14, off nt
	global_store_dword v[32:33], v15, off nt
	global_store_dword v[34:35], v16, off nt
	global_store_dword v[36:37], v17, off nt
	s_and_saveexec_b64 s[2:3], vcc
	s_cbranch_execz .LBB2_139
	v_add_u32_e32 v14, s18, v24
	v_mad_i64_i32 v[14:15], s[14:15], v14, s34, 0
	v_lshl_add_u64 v[14:15], v[14:15], 2, v[18:19]
	v_add_f32_e32 v6, v6, v114
	global_store_dword v[14:15], v6, off nt
.LBB2_139:
	s_or_b64 exec, exec, s[2:3]
	v_or_b32_e32 v6, 17, v22
	v_cmp_gt_u32_e64 s[2:3], 20, v6
	s_and_saveexec_b64 s[14:15], s[2:3]
	s_cbranch_execz .LBB2_141
	v_add_u32_e32 v6, s18, v6
	v_mad_i64_i32 v[14:15], s[2:3], v6, s34, 0
	v_add_f32_e32 v16, v7, v115
	v_lshl_add_u64 v[6:7], v[14:15], 2, v[18:19]
	global_store_dword v[6:7], v16, off nt
.LBB2_141:
	s_or_b64 exec, exec, s[14:15]
	v_or_b32_e32 v6, 18, v22
	v_cmp_gt_u32_e64 s[2:3], 20, v6
	s_and_saveexec_b64 s[14:15], s[2:3]
	s_cbranch_execz .LBB2_143
	v_add_u32_e32 v6, s18, v6
	v_mad_i64_i32 v[6:7], s[2:3], v6, s34, 0
	v_lshl_add_u64 v[6:7], v[6:7], 2, v[18:19]
	v_add_f32_e32 v8, v8, v116
	global_store_dword v[6:7], v8, off nt

.LBB2_162:
	v_lshlrev_b32_e32 v8, 2, v22
	global_load_dwordx4 v[16:19], v8, s[20:21]
	v_add_u32_e32 v15, s18, v22
	v_lshl_add_u64 v[6:7], v[0:1], 2, s[4:5]
	v_mov_b32_e32 v9, 0
	v_or_b32_e32 v14, 16, v22
	v_mad_i64_i32 v[20:21], s[0:1], v15, s34, 0
	v_add_u32_e32 v23, 1, v15
	v_add_u32_e32 v26, 2, v15
	v_add_u32_e32 v15, 3, v15
	v_lshl_add_u64 v[8:9], s[20:21], 0, v[8:9]
	v_lshl_add_u64 v[20:21], v[20:21], 2, v[6:7]
	v_mad_i64_i32 v[24:25], s[0:1], v23, s34, 0
	v_mad_i64_i32 v[26:27], s[0:1], v26, s34, 0
	v_mad_i64_i32 v[28:29], s[0:1], v15, s34, 0
	v_cmp_gt_u32_e32 vcc, 20, v14
	v_lshl_add_u64 v[24:25], v[24:25], 2, v[6:7]
	v_lshl_add_u64 v[26:27], v[26:27], 2, v[6:7]
	v_lshl_add_u64 v[28:29], v[28:29], 2, v[6:7]
	s_and_saveexec_b64 s[68:69], vcc
	global_load_dword v117, v[8:9], off offset:64
	global_load_dword v118, v[8:9], off offset:68
	global_load_dword v119, v[8:9], off offset:72
	s_mov_b64 exec, s[68:69]
	s_waitcnt vmcnt(0)
	v_add_f32_e32 v10, v10, v16
	v_add_f32_e32 v11, v11, v17
	v_add_f32_e32 v12, v12, v18
	v_add_f32_e32 v13, v13, v19
	global_store_dword v[20:21], v10, off nt
	global_store_dword v[24:25], v11, off nt
	global_store_dword v[26:27], v12, off nt
	global_store_dword v[28:29], v13, off nt
	s_and_saveexec_b64 s[0:1], vcc
	s_cbranch_execz .LBB2_164
	v_add_u32_e32 v10, s18, v14
	v_mad_i64_i32 v[10:11], s[6:7], v10, s34, 0
	v_lshl_add_u64 v[10:11], v[10:11], 2, v[6:7]
	v_add_f32_e32 v2, v2, v117
	global_store_dword v[10:11], v2, off nt
.LBB2_164:
	s_or_b64 exec, exec, s[0:1]
	v_or_b32_e32 v2, 17, v22
	v_cmp_gt_u32_e64 s[0:1], 20, v2
	s_and_saveexec_b64 s[6:7], s[0:1]
	s_cbranch_execz .LBB2_166
	v_add_u32_e32 v2, s18, v2
	v_mad_i64_i32 v[10:11], s[0:1], v2, s34, 0
	v_add_f32_e32 v12, v3, v118
	v_lshl_add_u64 v[2:3], v[10:11], 2, v[6:7]
	global_store_dword v[2:3], v12, off nt
.LBB2_166:
	s_or_b64 exec, exec, s[6:7]
	v_or_b32_e32 v2, 18, v22
	v_cmp_gt_u32_e64 s[0:1], 20, v2
	s_and_saveexec_b64 s[6:7], s[0:1]
	s_cbranch_execz .LBB2_168
	v_add_u32_e32 v2, s18, v2
	v_mad_i64_i32 v[2:3], s[0:1], v2, s34, 0
	v_lshl_add_u64 v[2:3], v[2:3], 2, v[6:7]
	v_add_f32_e32 v4, v4, v119
	global_store_dword v[2:3], v4, off nt

	.amdhsa_kernel _Z10head_fusedPKDF16_S0_S0_PKfS2_S2_S2_S2_S2_S2_S2_Pf
		.amdhsa_group_segment_fixed_size 49152
		.amdhsa_private_segment_fixed_size 0
		.amdhsa_kernarg_size 96
		.amdhsa_user_sgpr_count 2
		.amdhsa_user_sgpr_dispatch_ptr 0
		.amdhsa_user_sgpr_queue_ptr 0
		.amdhsa_user_sgpr_kernarg_segment_ptr 1
		.amdhsa_user_sgpr_dispatch_id 0
		.amdhsa_user_sgpr_kernarg_preload_length 0
		.amdhsa_user_sgpr_kernarg_preload_offset 0
		.amdhsa_user_sgpr_private_segment_size 0
		.amdhsa_uses_dynamic_stack 0
		.amdhsa_enable_private_segment 0
		.amdhsa_system_sgpr_workgroup_id_x 1
		.amdhsa_system_sgpr_workgroup_id_y 1
		.amdhsa_system_sgpr_workgroup_id_z 0
		.amdhsa_system_sgpr_workgroup_info 0
		.amdhsa_system_vgpr_workitem_id 0
		.amdhsa_next_free_vgpr 120
		.amdhsa_next_free_sgpr 91
		.amdhsa_accum_offset 120
		.amdhsa_reserve_vcc 1
		.amdhsa_float_round_mode_32 0
		.amdhsa_float_round_mode_16_64 0
		.amdhsa_float_denorm_mode_32 3
		.amdhsa_float_denorm_mode_16_64 3
		.amdhsa_dx10_clamp 1
		.amdhsa_ieee_mode 1
		.amdhsa_fp16_overflow 0
		.amdhsa_tg_split 0
		.amdhsa_exception_fp_ieee_invalid_op 0
		.amdhsa_exception_fp_denorm_src 0
		.amdhsa_exception_fp_ieee_div_zero 0
		.amdhsa_exception_fp_ieee_overflow 0
		.amdhsa_exception_fp_ieee_underflow 0
		.amdhsa_exception_fp_ieee_inexact 0
		.amdhsa_exception_int_div_zero 0
	.end_amdhsa_kernel

amdhsa.kernels:
  - .agpr_count:     0
    .args:
      - .offset:         0
        .size:           40
        .value_kind:     by_value
      - .actual_access:  read_only
        .address_space:  global
        .offset:         40
        .size:           8
        .value_kind:     global_buffer
      - .actual_access:  read_only
        .address_space:  global
        .offset:         48
        .size:           8
        .value_kind:     global_buffer
      - .actual_access:  read_only
        .address_space:  global
        .offset:         56
        .size:           8
        .value_kind:     global_buffer
      - .actual_access:  read_only
        .address_space:  global
        .offset:         64
        .size:           8
        .value_kind:     global_buffer
      - .actual_access:  read_only
        .address_space:  global
        .offset:         72
        .size:           8
        .value_kind:     global_buffer
      - .actual_access:  write_only
        .address_space:  global
        .offset:         80
        .size:           8
        .value_kind:     global_buffer
      - .actual_access:  write_only
        .address_space:  global
        .offset:         88
        .size:           8
        .value_kind:     global_buffer
      - .actual_access:  write_only
        .address_space:  global
        .offset:         96
        .size:           8
        .value_kind:     global_buffer
    .group_segment_fixed_size: 16384
    .kernarg_segment_align: 8
    .kernarg_segment_size: 104
    .language:       OpenCL C
    .language_version:
      - 2
      - 0
    .max_flat_workgroup_size: 256
    .name:           _Z8prep_all8FeatPtrsPKfS1_S1_S1_S1_PDF16_S2_S2_
    .private_segment_fixed_size: 0
    .sgpr_count:     26
    .sgpr_spill_count: 0
    .symbol:         _Z8prep_all8FeatPtrsPKfS1_S1_S1_S1_PDF16_S2_S2_.kd
    .uniform_work_group_size: 1
    .uses_dynamic_stack: false
    .vgpr_count:     38
    .vgpr_spill_count: 0
    .wavefront_size: 64
  - .agpr_count:     0
    .args:
      - .address_space:  global
        .offset:         0
        .size:           8
        .value_kind:     global_buffer
      - .address_space:  global
        .offset:         8
        .size:           8
        .value_kind:     global_buffer
      - .actual_access:  read_only
        .address_space:  global
        .offset:         16
        .size:           8
        .value_kind:     global_buffer
      - .actual_access:  write_only
        .address_space:  global
        .offset:         24
        .size:           8
        .value_kind:     global_buffer
      - .actual_access:  write_only
        .address_space:  global
        .offset:         32
        .size:           8
        .value_kind:     global_buffer
      - .offset:         40
        .size:           4
        .value_kind:     by_value
      - .offset:         44
        .size:           4
        .value_kind:     by_value
      - .address_space:  global
        .offset:         48
        .size:           8
        .value_kind:     global_buffer
      - .actual_access:  read_only
        .address_space:  global
        .offset:         56
        .size:           8
        .value_kind:     global_buffer
      - .offset:         64
        .size:           4
        .value_kind:     by_value
      - .actual_access:  read_only
        .address_space:  global
        .offset:         72
        .size:           8
        .value_kind:     global_buffer
      - .actual_access:  read_only
        .address_space:  global
        .offset:         80
        .size:           8
        .value_kind:     global_buffer
      - .offset:         88
        .size:           4
        .value_kind:     hidden_block_count_x
      - .offset:         92
        .size:           4
        .value_kind:     hidden_block_count_y
      - .offset:         96
        .size:           4
        .value_kind:     hidden_block_count_z
      - .offset:         100
        .size:           2
        .value_kind:     hidden_group_size_x
      - .offset:         102
        .size:           2
        .value_kind:     hidden_group_size_y
      - .offset:         104
        .size:           2
        .value_kind:     hidden_group_size_z
      - .offset:         106
        .size:           2
        .value_kind:     hidden_remainder_x
      - .offset:         108
        .size:           2
        .value_kind:     hidden_remainder_y
      - .offset:         110
        .size:           2
        .value_kind:     hidden_remainder_z
      - .offset:         128
        .size:           8
        .value_kind:     hidden_global_offset_x
      - .offset:         136
        .size:           8
        .value_kind:     hidden_global_offset_y
      - .offset:         144
        .size:           8
        .value_kind:     hidden_global_offset_z
      - .offset:         152
        .size:           2
        .value_kind:     hidden_grid_dims
      - .offset:         208
        .size:           4
        .value_kind:     hidden_dynamic_lds_size
    .group_segment_fixed_size: 0
    .kernarg_segment_align: 8
    .kernarg_segment_size: 344
    .language:       OpenCL C
    .language_version:
      - 2
      - 0
    .max_flat_workgroup_size: 512
    .name:           _Z9conv_gemmPKDF16_S0_PKfPDF16_PfiiS3_S2_iS2_S2_
    .private_segment_fixed_size: 0
    .sgpr_count:     78
    .sgpr_spill_count: 0
    .symbol:         _Z9conv_gemmPKDF16_S0_PKfPDF16_PfiiS3_S2_iS2_S2_.kd
    .uniform_work_group_size: 1
    .uses_dynamic_stack: false
    .vgpr_count:     256
    .vgpr_spill_count: 0
    .wavefront_size: 64
  - .agpr_count:     0
    .args:
      - .actual_access:  read_only
        .address_space:  global
        .offset:         0
        .size:           8
        .value_kind:     global_buffer
      - .actual_access:  read_only
        .address_space:  global
        .offset:         8
        .size:           8
        .value_kind:     global_buffer
      - .actual_access:  read_only
        .address_space:  global
        .offset:         16
        .size:           8
        .value_kind:     global_buffer
      - .actual_access:  read_only
        .address_space:  global
        .offset:         24
        .size:           8
        .value_kind:     global_buffer
      - .actual_access:  read_only
        .address_space:  global
        .offset:         32
        .size:           8
        .value_kind:     global_buffer
      - .actual_access:  read_only
        .address_space:  global
        .offset:         40
        .size:           8
        .value_kind:     global_buffer
      - .actual_access:  read_only
        .address_space:  global
        .offset:         48
        .size:           8
        .value_kind:     global_buffer
      - .actual_access:  read_only
        .address_space:  global
        .offset:         56
        .size:           8
        .value_kind:     global_buffer
      - .actual_access:  read_only
        .address_space:  global
        .offset:         64
        .size:           8
        .value_kind:     global_buffer
      - .actual_access:  read_only
        .address_space:  global
        .offset:         72
        .size:           8
        .value_kind:     global_buffer
      - .actual_access:  read_only
        .address_space:  global
        .offset:         80
        .size:           8
        .value_kind:     global_buffer
      - .actual_access:  write_only
        .address_space:  global
        .offset:         88
        .size:           8
        .value_kind:     global_buffer
    .group_segment_fixed_size: 49152
    .kernarg_segment_align: 8
    .kernarg_segment_size: 96
    .language:       OpenCL C
    .language_version:
      - 2
      - 0
    .max_flat_workgroup_size: 512
    .name:           _Z10head_fusedPKDF16_S0_S0_PKfS2_S2_S2_S2_S2_S2_S2_Pf
    .private_segment_fixed_size: 0
    .sgpr_count:     57
    .sgpr_spill_count: 0
    .symbol:         _Z10head_fusedPKDF16_S0_S0_PKfS2_S2_S2_S2_S2_S2_S2_Pf.kd
    .uniform_work_group_size: 1
    .uses_dynamic_stack: false
    .vgpr_count:     120
    .vgpr_spill_count: 0
    .wavefront_size: 64
